# prologue: gain loads of the two memory-token rmsnorm loops issued with the row loads (no serial round trips)
# baseline (speedup 1.0000x reference)
.LBB0_18:
	global_load_dwordx4 v[16:19], v[10:11], off offset:-2048
	global_load_dwordx4 v[20:23], v[10:11], off offset:-1024
	global_load_dwordx4 v[24:27], v[10:11], off
	global_load_dwordx4 v[28:31], v[10:11], off offset:1024
	global_load_dwordx4 v[32:35], v[6:7], off
	global_load_dwordx4 v[100:103], v[6:7], off offset:1024
	global_load_dwordx4 v[104:107], v[6:7], off offset:2048
	global_load_dwordx4 v[108:111], v[6:7], off offset:3072
	v_add_u32_e32 v4, s16, v4
	v_lshl_add_u64 v[10:11], v[10:11], 0, s[6:7]
	s_waitcnt vmcnt(7)
	v_mov_b32_e32 v42, v17
	s_waitcnt vmcnt(6)
	v_mov_b32_e32 v43, v21
	v_mov_b32_e32 v40, v16
	v_mov_b32_e32 v41, v20
	s_waitcnt vmcnt(5)
	v_mov_b32_e32 v50, v25
	s_waitcnt vmcnt(4)
	v_mov_b32_e32 v51, v29
	v_pk_mul_f32 v[42:43], v[42:43], v[42:43]
	v_mov_b32_e32 v36, v18
	v_mov_b32_e32 v37, v22
	v_mov_b32_e32 v48, v24
	v_mov_b32_e32 v49, v28
	v_pk_mul_f32 v[50:51], v[50:51], v[50:51]
	v_pk_fma_f32 v[40:41], v[40:41], v[40:41], v[42:43]
	v_mov_b32_e32 v38, v19
	v_mov_b32_e32 v39, v23
	v_mov_b32_e32 v44, v26
	v_mov_b32_e32 v45, v30
	v_pk_fma_f32 v[42:43], v[48:49], v[48:49], v[50:51]
	v_pk_fma_f32 v[36:37], v[36:37], v[36:37], v[40:41]
	v_mov_b32_e32 v46, v27
	v_mov_b32_e32 v47, v31
	v_pk_fma_f32 v[40:41], v[44:45], v[44:45], v[42:43]
	v_pk_fma_f32 v[36:37], v[38:39], v[38:39], v[36:37]
	v_pk_fma_f32 v[38:39], v[46:47], v[46:47], v[40:41]
	v_add_f32_e32 v36, v36, v37
	v_add_f32_e32 v36, v36, v38
	v_add_f32_e32 v36, v36, v39
	ds_bpermute_b32 v37, v1, v36
	s_waitcnt lgkmcnt(0)
	v_add_f32_e32 v36, v36, v37
	ds_bpermute_b32 v37, v3, v36
	s_waitcnt lgkmcnt(0)
	v_add_f32_e32 v36, v36, v37
	ds_bpermute_b32 v37, v12, v36
	s_waitcnt lgkmcnt(0)
	v_add_f32_e32 v36, v36, v37
	ds_bpermute_b32 v37, v13, v36
	s_waitcnt lgkmcnt(0)
	v_add_f32_e32 v36, v36, v37
	ds_bpermute_b32 v37, v14, v36
	s_waitcnt lgkmcnt(0)
	v_add_f32_e32 v36, v36, v37
	ds_bpermute_b32 v37, v15, v36
	s_waitcnt lgkmcnt(0)
	v_add_f32_e32 v36, v36, v37
	v_fmamk_f32 v36, v36, 0x3a800000, v5
	v_mul_f32_e32 v37, 0x4b800000, v36
	v_cmp_gt_f32_e32 vcc, s15, v36
	s_nop 1
	v_cndmask_b32_e32 v36, v36, v37, vcc
	v_rsq_f32_e32 v36, v36
	s_nop 0
	v_mul_f32_e32 v37, 0x45800000, v36
	v_cndmask_b32_e32 v36, v36, v37, vcc
	v_pk_mul_f32 v[16:17], v[16:17], v[36:37] op_sel_hi:[1,0]
	v_pk_mul_f32 v[18:19], v[18:19], v[36:37] op_sel_hi:[1,0]
	s_waitcnt vmcnt(0)
	v_pk_mul_f32 v[16:17], v[32:33], v[16:17]
	v_pk_mul_f32 v[18:19], v[34:35], v[18:19]
	v_cvt_pk_bf16_f32 v16, v16, v17
	v_cvt_pk_bf16_f32 v17, v18, v19
	global_store_dwordx2 v[8:9], v[16:17], off
	v_pk_mul_f32 v[20:21], v[20:21], v[36:37] op_sel_hi:[1,0]
	v_pk_mul_f32 v[22:23], v[22:23], v[36:37] op_sel_hi:[1,0]
	v_cmp_lt_i32_e32 vcc, s14, v4
	s_or_b64 s[8:9], vcc, s[8:9]
	v_pk_mul_f32 v[16:17], v[100:101], v[20:21]
	v_pk_mul_f32 v[18:19], v[102:103], v[22:23]
	v_cvt_pk_bf16_f32 v16, v16, v17
	v_cvt_pk_bf16_f32 v17, v18, v19
	global_store_dwordx2 v[8:9], v[16:17], off offset:512
	v_pk_mul_f32 v[20:21], v[24:25], v[36:37] op_sel_hi:[1,0]
	v_pk_mul_f32 v[22:23], v[26:27], v[36:37] op_sel_hi:[1,0]
	v_pk_mul_f32 v[16:17], v[104:105], v[20:21]
	v_pk_mul_f32 v[18:19], v[22:23], v[106:107]
	v_cvt_pk_bf16_f32 v16, v16, v17
	v_cvt_pk_bf16_f32 v17, v18, v19
	global_store_dwordx2 v[8:9], v[16:17], off offset:1024
	v_pk_mul_f32 v[20:21], v[28:29], v[36:37] op_sel_hi:[1,0]
	v_pk_mul_f32 v[22:23], v[30:31], v[36:37] op_sel_hi:[1,0]
	v_pk_mul_f32 v[16:17], v[20:21], v[108:109]
	v_pk_mul_f32 v[18:19], v[22:23], v[110:111]
	v_cvt_pk_bf16_f32 v16, v16, v17
	v_cvt_pk_bf16_f32 v17, v18, v19
	global_store_dwordx2 v[8:9], v[16:17], off offset:1536
	v_lshl_add_u64 v[8:9], v[8:9], 0, s[4:5]
	s_andn2_b64 exec, exec, s[8:9]
	s_cbranch_execnz .LBB0_18

.LBB0_21:
	global_load_dwordx4 v[22:25], v[16:17], off offset:-2048
	global_load_dwordx4 v[26:29], v[16:17], off offset:-1024
	global_load_dwordx4 v[30:33], v[16:17], off
	global_load_dwordx4 v[34:37], v[16:17], off offset:1024
	global_load_dwordx4 v[38:41], v[6:7], off
	global_load_dwordx4 v[100:103], v[8:9], off
	global_load_dwordx4 v[104:107], v[10:11], off
	global_load_dwordx4 v[108:111], v[12:13], off
	v_add_u32_e32 v4, s16, v4
	v_lshl_add_u64 v[16:17], v[16:17], 0, s[6:7]
	s_waitcnt vmcnt(7)
	v_mov_b32_e32 v48, v23
	s_waitcnt vmcnt(6)
	v_mov_b32_e32 v49, v27
	v_mov_b32_e32 v46, v22
	v_mov_b32_e32 v47, v26
	s_waitcnt vmcnt(5)
	v_mov_b32_e32 v56, v31
	s_waitcnt vmcnt(4)
	v_mov_b32_e32 v57, v35
	v_pk_mul_f32 v[48:49], v[48:49], v[48:49]
	v_mov_b32_e32 v42, v24
	v_mov_b32_e32 v43, v28
	v_mov_b32_e32 v54, v30
	v_mov_b32_e32 v55, v34
	v_pk_mul_f32 v[56:57], v[56:57], v[56:57]
	v_pk_fma_f32 v[46:47], v[46:47], v[46:47], v[48:49]
	v_mov_b32_e32 v44, v25
	v_mov_b32_e32 v45, v29
	v_mov_b32_e32 v50, v32
	v_mov_b32_e32 v51, v36
	v_pk_fma_f32 v[48:49], v[54:55], v[54:55], v[56:57]
	v_pk_fma_f32 v[42:43], v[42:43], v[42:43], v[46:47]
	v_mov_b32_e32 v52, v33
	v_mov_b32_e32 v53, v37
	v_pk_fma_f32 v[46:47], v[50:51], v[50:51], v[48:49]
	v_pk_fma_f32 v[42:43], v[44:45], v[44:45], v[42:43]
	v_pk_fma_f32 v[44:45], v[52:53], v[52:53], v[46:47]
	v_add_f32_e32 v42, v42, v43
	v_add_f32_e32 v42, v42, v44
	v_add_f32_e32 v42, v42, v45
	ds_bpermute_b32 v43, v1, v42
	s_waitcnt lgkmcnt(0)
	v_add_f32_e32 v42, v42, v43
	ds_bpermute_b32 v43, v3, v42
	s_waitcnt lgkmcnt(0)
	v_add_f32_e32 v42, v42, v43
	ds_bpermute_b32 v43, v18, v42
	s_waitcnt lgkmcnt(0)
	v_add_f32_e32 v42, v42, v43
	ds_bpermute_b32 v43, v19, v42
	s_waitcnt lgkmcnt(0)
	v_add_f32_e32 v42, v42, v43
	ds_bpermute_b32 v43, v20, v42
	s_waitcnt lgkmcnt(0)
	v_add_f32_e32 v42, v42, v43
	ds_bpermute_b32 v43, v21, v42
	s_waitcnt lgkmcnt(0)
	v_add_f32_e32 v42, v42, v43
	v_fmamk_f32 v42, v42, 0x3a800000, v5
	v_mul_f32_e32 v43, 0x4b800000, v42
	v_cmp_gt_f32_e32 vcc, s14, v42
	s_nop 1
	v_cndmask_b32_e32 v42, v42, v43, vcc
	v_rsq_f32_e32 v42, v42
	s_nop 0
	v_mul_f32_e32 v43, 0x45800000, v42
	v_cndmask_b32_e32 v42, v42, v43, vcc
	v_pk_mul_f32 v[22:23], v[22:23], v[42:43] op_sel_hi:[1,0]
	v_pk_mul_f32 v[24:25], v[24:25], v[42:43] op_sel_hi:[1,0]
	s_waitcnt vmcnt(0)
	v_pk_mul_f32 v[22:23], v[38:39], v[22:23]
	v_pk_mul_f32 v[24:25], v[40:41], v[24:25]
	v_cvt_pk_bf16_f32 v22, v22, v23
	v_cvt_pk_bf16_f32 v23, v24, v25
	global_store_dwordx2 v[14:15], v[22:23], off
	v_pk_mul_f32 v[26:27], v[26:27], v[42:43] op_sel_hi:[1,0]
	v_pk_mul_f32 v[28:29], v[28:29], v[42:43] op_sel_hi:[1,0]
	v_cmp_lt_i32_e32 vcc, s15, v4
	s_or_b64 s[8:9], vcc, s[8:9]
	v_pk_mul_f32 v[22:23], v[100:101], v[26:27]
	v_pk_mul_f32 v[24:25], v[102:103], v[28:29]
	v_cvt_pk_bf16_f32 v22, v22, v23
	v_cvt_pk_bf16_f32 v23, v24, v25
	global_store_dwordx2 v[14:15], v[22:23], off offset:512
	v_pk_mul_f32 v[26:27], v[30:31], v[42:43] op_sel_hi:[1,0]
	v_pk_mul_f32 v[28:29], v[32:33], v[42:43] op_sel_hi:[1,0]
	v_pk_mul_f32 v[22:23], v[104:105], v[26:27]
	v_pk_mul_f32 v[24:25], v[28:29], v[106:107]
	v_cvt_pk_bf16_f32 v22, v22, v23
	v_cvt_pk_bf16_f32 v23, v24, v25
	global_store_dwordx2 v[14:15], v[22:23], off offset:1024
	v_pk_mul_f32 v[26:27], v[34:35], v[42:43] op_sel_hi:[1,0]
	v_pk_mul_f32 v[28:29], v[36:37], v[42:43] op_sel_hi:[1,0]
	v_pk_mul_f32 v[22:23], v[26:27], v[108:109]
	v_pk_mul_f32 v[24:25], v[28:29], v[110:111]
	v_cvt_pk_bf16_f32 v22, v22, v23
	v_cvt_pk_bf16_f32 v23, v24, v25
	global_store_dwordx2 v[14:15], v[22:23], off offset:1536
	v_lshl_add_u64 v[14:15], v[14:15], 0, s[4:5]
	s_andn2_b64 exec, exec, s[8:9]
	s_cbranch_execnz .LBB0_21
